# stagger of the second WG per CU in in-proj phases reduced from 1792 to 896 cycles (hand-written in-proj loop unchanged)
# speedup vs baseline: 1.0167x; 1.0020x over previous
; #define PR_BEGIN(id) do { if (PROBE_SP == (id)) c.prt = __builtin_amdgcn_s_memrealtime(); } while (0)
; #define PR_END(id) do { if (PROBE_SP == (id)) c.pracc += __builtin_amdgcn_s_memrealtime() - c.prt; } while (0)
; __global__ void __launch_bounds__(NTHR, 2) mk_fwd(Params prm) {
;     ...
;     for (int ph = prm.ph_lo; ph < prm.ph_hi; ++ph) {
;         if (PROBE_SP >= 0) pr_t0 = __builtin_amdgcn_s_memrealtime();
;         asm volatile("" : "+s"(c.p));
;         { int t_ = threadIdx.x; asm volatile("" : "+v"(t_)); c.tid = t_; }
;         if (ph == 0) {
;             const bool split = G >= 384;
;             const int g2 = split ? (bid >= 256 ? gtid - 65536 : 0x3fffffff) : gtid, gth2 = split ? gthreads - 65536 : gthreads;
;             ph_prep(c, g2, gth2, bid, G, (float*)smem_raw); PR_BEGIN(124); cvt_small(c, g2, gth2); PR_END(124); }
;         else if (ph == 1) ph_norm1(c, 0, gw, nwaves, smem_raw);
;         else {
;             const int layer = (ph - 2) / PH_PER_LAYER, sp = (ph - 2) % PH_PER_LAYER;
;             switch (sp) {
;             case 0: for (int t = bid; t < 136 * 18 + (layer == 0 ? 5120 : 0); t += G) { asm volatile("" : "+v"(c.tid)); if (t < 136 * 18) ph_inproj_mfma(c, layer, t, smem_raw); else ph_prepB(c, t - 136 * 18); } break;
.LBB0_13:
	s_lshr_b32 s6, 0x804, s66
	s_bitcmp1_b32 s6, 0
	s_cbranch_scc0 .Lstag_done
	ds_read_b32 v2, v146
	s_waitcnt lgkmcnt(0)
	v_readfirstlane_b32 s6, v2
	s_cmp_eq_u32 s6, 0
	s_cbranch_scc1 .Lstag_done
	s_sleep 14
